# P3 qknorm rows re-dealt: CUs 0-127 (S5 state GEMM CUs) one 4-row step per wave, CUs 128-255 three
# speedup vs baseline: 1.0016x; 1.0009x over previous
; __device__ __forceinline__ void qknorm_body(const Args& a, int wave, int lane, int G, int bid) {
;     ...
;         for (int row0 = gw; row0 < T; row0 += 4 * NGW) {
;             v4u qa[4], qb[4], ka[4];
; #pragma unroll
;             for (int u = 0; u < 4; ++u) { const int row = min(row0 + u * NGW, T - 1); const v4u* qp = (const v4u*)(Q + (size_t)row * 1024 + 16 * lane); qa[u] = qp[0]; qb[u] = qp[1]; ka[u] = *(const v4u*)(K + (size_t)row * 256 + 8 * l32); }
; #pragma unroll
;             for (int u = 0; u < 4; ++u) { const int row = row0 + u * NGW; if (row < T) {
.LBB0_611:
	s_add_i32 s3, s4, s14
	s_add_i32 s3, s3, s14
	s_add_i32 s3, s3, s14
	s_cmpk_lg_i32 s88, 0x100
	s_cbranch_scc1 .Lqk_generic
	s_cmpk_lt_i32 s84, 0x80
	s_cbranch_scc1 .LBB0_625
	s_mov_b32 s2, s3
	s_cmpk_lt_i32 s2, 0x4000
	s_cbranch_scc1 .LBB0_612
	s_sub_i32 s2, s4, s14
	s_bitcmp0_b32 s2, 10
	s_cbranch_scc1 .LBB0_625
	s_addk_i32 s2, 0xfc00
	s_branch .LBB0_612
.Lqk_generic:
	s_mov_b32 s2, s3
	s_cmpk_lt_i32 s2, 0x4000
	s_cbranch_scc0 .LBB0_625
